# ATT1 selected/window tile updates: K and V^T fragment LDS reads issued together up front into unused VGPRs, counted lgkmcnt waits
# speedup vs baseline: 1.0233x; 1.0233x over previous
.LBB0_1683:
	s_add_u32 s20, s8, -1
	s_add_i32 s12, s18, -2
	s_cmp_gt_u32 s12, s14
	v_lshrrev_b64 v[148:149], s20, v[144:145]
	s_cbranch_scc1 .LBB0_1691
	ds_read_b128 v[64:67], v152
	ds_read_b128 v[80:83], v152 offset:32
	ds_read_b128 v[224:227], v152 offset:64
	ds_read_b128 v[228:231], v152 offset:96
	ds_read_b64_tr_b16 v[232:233], v153 offset:4608
	ds_read_b64_tr_b16 v[234:235], v153 offset:5120
	ds_read_b64_tr_b16 v[236:237], v153 offset:5632
	ds_read_b64_tr_b16 v[238:239], v153 offset:6144
	ds_read_b64_tr_b16 v[240:241], v153 offset:6656
	ds_read_b64_tr_b16 v[242:243], v153 offset:7168
	ds_read_b64_tr_b16 v[244:245], v153 offset:7680
	ds_read_b64_tr_b16 v[246:247], v153 offset:8192
	s_add_i32 s2, s19, 0xffffffa0
	v_and_b32_e32 v84, 1, v148
	s_cmp_le_u32 s2, s15
	v_cmp_eq_u32_e64 s[0:1], 1, v84
	s_cselect_b64 s[6:7], -1, 0
	s_cmp_gt_u32 s2, s15
	s_waitcnt lgkmcnt(11)
	v_mfma_f32_32x32x16_bf16 v[64:79], v[64:67], v[128:131], 0
	s_waitcnt lgkmcnt(10)
	v_mfma_f32_32x32x16_bf16 v[64:79], v[80:83], v[132:135], v[64:79]
	s_waitcnt lgkmcnt(9)
	v_mfma_f32_32x32x16_bf16 v[64:79], v[224:227], v[136:139], v[64:79]
	s_waitcnt lgkmcnt(8)
	v_mfma_f32_32x32x16_bf16 v[64:79], v[228:231], v[140:143], v[64:79]
	s_cbranch_scc1 .LBB0_1692
	v_mov_b32_e32 v80, 0x7f800000
	s_and_saveexec_b64 s[2:3], s[0:1]
	s_cbranch_execz .LBB0_1689
	s_mov_b32 s10, 0xff800000
	v_cmp_neq_f32_e32 vcc, s10, v155
	v_mov_b32_e32 v80, 0
	s_and_saveexec_b64 s[10:11], vcc
	v_mov_b32_e32 v80, v155
	s_or_b64 exec, exec, s[10:11]

.LBB0_1702:
	v_cvt_pk_bf16_f32 v64, v160, v158
	v_cvt_pk_bf16_f32 v65, v165, v157
	v_cvt_pk_bf16_f32 v66, v166, v161
	v_cvt_pk_bf16_f32 v67, v167, v159
	v_cvt_pk_bf16_f32 v68, v168, v163
	v_cvt_pk_bf16_f32 v69, v169, v162
	s_waitcnt lgkmcnt(6)
	v_mfma_f32_32x32x16_bf16 v[48:63], v[232:235], v[64:67], v[48:63]
	v_cvt_pk_bf16_f32 v70, v170, v164
	v_cvt_pk_bf16_f32 v71, v171, v156
	v_add_f32_e32 v194, v194, v93
	s_waitcnt lgkmcnt(4)
	v_mfma_f32_32x32x16_bf16 v[48:63], v[236:239], v[68:71], v[48:63]
	s_waitcnt lgkmcnt(2)
	v_mfma_f32_32x32x16_bf16 v[32:47], v[240:243], v[64:67], v[32:47]
	s_waitcnt lgkmcnt(0)
	v_mfma_f32_32x32x16_bf16 v[32:47], v[244:247], v[68:71], v[32:47]
.LBB0_1703:
	s_add_u32 s6, s8, 2
	s_addc_u32 s7, s9, 0
	s_min_i32 s0, s6, s16
	s_mul_i32 s64, s0, 0x28000
	s_waitcnt vmcnt(3)
	ds_write_b128 v150, v[96:99] offset:34816
	s_waitcnt vmcnt(2)
	ds_write_b128 v151, v[100:103] offset:39424
	s_waitcnt vmcnt(1)
	ds_write_b128 v150, v[104:107] offset:43520
	s_waitcnt vmcnt(0)
	ds_write_b128 v151, v[108:111] offset:48128
	v_lshl_add_u64 v[64:65], s[64:65], 1, v[146:147]
	global_load_dwordx4 v[96:99], v[64:65], off offset:3072
	global_load_dwordx4 v[100:103], v[64:65], off offset:3584
	v_add_co_u32_e32 v64, vcc, 0x28000, v64
	s_cmp_ge_u32 s12, s14
	s_nop 0
	v_addc_co_u32_e32 v65, vcc, 0, v65, vcc
	global_load_dwordx4 v[104:107], v[64:65], off offset:3072
	global_load_dwordx4 v[108:111], v[64:65], off offset:3584
	s_cbranch_scc1 .LBB0_1711
	ds_read_b128 v[64:67], v152 offset:8704
	ds_read_b128 v[80:83], v152 offset:8736
	ds_read_b128 v[224:227], v152 offset:8768
	ds_read_b128 v[228:231], v152 offset:8800
	ds_read_b64_tr_b16 v[232:233], v153 offset:13312
	ds_read_b64_tr_b16 v[234:235], v153 offset:13824
	ds_read_b64_tr_b16 v[236:237], v153 offset:14336
	ds_read_b64_tr_b16 v[238:239], v153 offset:14848
	ds_read_b64_tr_b16 v[240:241], v153 offset:15360
	ds_read_b64_tr_b16 v[242:243], v153 offset:15872
	ds_read_b64_tr_b16 v[244:245], v153 offset:16384
	ds_read_b64_tr_b16 v[246:247], v153 offset:16896
	s_sub_i32 s2, s19, 64
	v_and_b32_e32 v84, 1, v148
	s_cmp_le_u32 s2, s15
	v_cmp_eq_u32_e64 s[0:1], 1, v84
	s_cselect_b64 s[10:11], -1, 0
	s_cmp_gt_u32 s2, s15
	s_waitcnt lgkmcnt(11)
	v_mfma_f32_32x32x16_bf16 v[64:79], v[64:67], v[128:131], 0
	s_waitcnt lgkmcnt(10)
	v_mfma_f32_32x32x16_bf16 v[64:79], v[80:83], v[132:135], v[64:79]
	s_waitcnt lgkmcnt(9)
	v_mfma_f32_32x32x16_bf16 v[64:79], v[224:227], v[136:139], v[64:79]
	s_waitcnt lgkmcnt(8)
	v_mfma_f32_32x32x16_bf16 v[64:79], v[228:231], v[140:143], v[64:79]
	s_cbranch_scc1 .LBB0_1712
	v_mov_b32_e32 v80, 0x7f800000
	s_and_saveexec_b64 s[2:3], s[0:1]
	s_cbranch_execz .LBB0_1709
	s_mov_b32 s9, 0xff800000
	v_cmp_neq_f32_e32 vcc, s9, v149
	v_mov_b32_e32 v80, 0
	s_and_saveexec_b64 s[12:13], vcc
	v_mov_b32_e32 v80, v149
	s_or_b64 exec, exec, s[12:13]

.LBB0_1722:
	v_cvt_pk_bf16_f32 v64, v159, v157
	v_cvt_pk_bf16_f32 v65, v164, v156
	v_cvt_pk_bf16_f32 v66, v165, v160
	v_cvt_pk_bf16_f32 v67, v166, v158
	v_cvt_pk_bf16_f32 v68, v167, v162
	v_cvt_pk_bf16_f32 v69, v168, v161
	s_waitcnt lgkmcnt(6)
	v_mfma_f32_32x32x16_bf16 v[48:63], v[232:235], v[64:67], v[48:63]
	v_cvt_pk_bf16_f32 v70, v169, v163
	v_cvt_pk_bf16_f32 v71, v170, v148
	v_add_f32_e32 v194, v194, v93
	s_waitcnt lgkmcnt(4)
	v_mfma_f32_32x32x16_bf16 v[48:63], v[236:239], v[68:71], v[48:63]
	s_waitcnt lgkmcnt(2)
	v_mfma_f32_32x32x16_bf16 v[32:47], v[240:243], v[64:67], v[32:47]
	s_waitcnt lgkmcnt(0)
	v_mfma_f32_32x32x16_bf16 v[32:47], v[244:247], v[68:71], v[32:47]
.LBB0_1723:
	s_mov_b64 s[0:1], -1
	s_cmp_ge_u32 s20, s16
	v_readfirstlane_b32 s2, v0
	v_readfirstlane_b32 s3, v0
	s_waitcnt lgkmcnt(0)
	s_barrier
	s_cbranch_scc1 .LBB0_1681
	s_cmp_gt_u32 s18, s14
	v_lshrrev_b64 v[148:149], s8, v[144:145]
	s_cbranch_scc1 .LBB0_1732
	ds_read_b128 v[64:67], v152 offset:34816
	ds_read_b128 v[80:83], v152 offset:34848
	ds_read_b128 v[224:227], v152 offset:34880
	ds_read_b128 v[228:231], v152 offset:34912
	ds_read_b64_tr_b16 v[232:233], v153 offset:39424
	ds_read_b64_tr_b16 v[234:235], v153 offset:39936
	ds_read_b64_tr_b16 v[236:237], v153 offset:40448
	ds_read_b64_tr_b16 v[238:239], v153 offset:40960
	ds_read_b64_tr_b16 v[240:241], v153 offset:41472
	ds_read_b64_tr_b16 v[242:243], v153 offset:41984
	ds_read_b64_tr_b16 v[244:245], v153 offset:42496
	ds_read_b64_tr_b16 v[246:247], v153 offset:43008
	s_sub_i32 s2, s19, 32
	v_and_b32_e32 v84, 1, v148
	s_cmp_le_u32 s2, s15
	v_cmp_eq_u32_e64 s[0:1], 1, v84
	s_cselect_b64 s[10:11], -1, 0
	s_cmp_gt_u32 s2, s15
	s_waitcnt lgkmcnt(11)
	v_mfma_f32_32x32x16_bf16 v[64:79], v[64:67], v[128:131], 0
	s_waitcnt lgkmcnt(10)
	v_mfma_f32_32x32x16_bf16 v[64:79], v[80:83], v[132:135], v[64:79]
	s_waitcnt lgkmcnt(9)
	v_mfma_f32_32x32x16_bf16 v[64:79], v[224:227], v[136:139], v[64:79]
	s_waitcnt lgkmcnt(8)
	v_mfma_f32_32x32x16_bf16 v[64:79], v[228:231], v[140:143], v[64:79]
	s_cbranch_scc1 .LBB0_1737
	v_mov_b32_e32 v80, 0x7f800000
	s_and_saveexec_b64 s[2:3], s[0:1]
	s_cbranch_execz .LBB0_1730
	s_mov_b32 s9, 0xff800000
	v_cmp_neq_f32_e32 vcc, s9, v155
	v_mov_b32_e32 v80, 0
	s_and_saveexec_b64 s[12:13], vcc
	v_mov_b32_e32 v80, v155
	s_or_b64 exec, exec, s[12:13]

.LBB0_1748:
	s_add_i32 s0, s8, 3
	s_min_i32 s0, s0, s16
	s_mul_i32 s64, s0, 0x28000
	s_waitcnt vmcnt(7)
	ds_write_b128 v150, v[112:115]
	s_waitcnt vmcnt(6)
	ds_write_b128 v151, v[116:119] offset:4608
	s_waitcnt vmcnt(5)
	ds_write_b128 v150, v[124:127] offset:8704
	s_waitcnt vmcnt(4)
	ds_write_b128 v151, v[120:123] offset:13312
	v_lshl_add_u64 v[64:65], s[64:65], 1, v[146:147]
	global_load_dwordx4 v[112:115], v[64:65], off offset:3072
	global_load_dwordx4 v[116:119], v[64:65], off offset:3584
	v_add_co_u32_e32 v64, vcc, 0x28000, v64
	s_cmp_ge_u32 s18, s14
	s_nop 0
	v_addc_co_u32_e32 v65, vcc, 0, v65, vcc
	global_load_dwordx4 v[124:127], v[64:65], off offset:3072
	global_load_dwordx4 v[120:123], v[64:65], off offset:3584
	s_cbranch_scc1 .LBB0_1756
	ds_read_b128 v[64:67], v152 offset:43520
	ds_read_b128 v[80:83], v152 offset:43552
	ds_read_b128 v[224:227], v152 offset:43584
	ds_read_b128 v[228:231], v152 offset:43616
	ds_read_b64_tr_b16 v[232:233], v153 offset:48128
	ds_read_b64_tr_b16 v[234:235], v153 offset:48640
	ds_read_b64_tr_b16 v[236:237], v153 offset:49152
	ds_read_b64_tr_b16 v[238:239], v153 offset:49664
	ds_read_b64_tr_b16 v[240:241], v153 offset:50176
	ds_read_b64_tr_b16 v[242:243], v153 offset:50688
	ds_read_b64_tr_b16 v[244:245], v153 offset:51200
	ds_read_b64_tr_b16 v[246:247], v153 offset:51712
	v_and_b32_e32 v84, 1, v148
	s_cmp_le_u32 s19, s15
	v_cmp_eq_u32_e64 s[0:1], 1, v84
	s_cselect_b64 s[8:9], -1, 0
	s_cmp_gt_u32 s19, s15
	s_waitcnt lgkmcnt(11)
	v_mfma_f32_32x32x16_bf16 v[64:79], v[64:67], v[128:131], 0
	s_waitcnt lgkmcnt(10)
	v_mfma_f32_32x32x16_bf16 v[64:79], v[80:83], v[132:135], v[64:79]
	s_waitcnt lgkmcnt(9)
	v_mfma_f32_32x32x16_bf16 v[64:79], v[224:227], v[136:139], v[64:79]
	s_waitcnt lgkmcnt(8)
	v_mfma_f32_32x32x16_bf16 v[64:79], v[228:231], v[140:143], v[64:79]
	s_cbranch_scc1 .LBB0_1757
	v_mov_b32_e32 v80, 0x7f800000
	s_and_saveexec_b64 s[2:3], s[0:1]
	s_cbranch_execz .LBB0_1754
	s_mov_b32 s10, 0xff800000
	v_cmp_neq_f32_e32 vcc, s10, v149
	v_mov_b32_e32 v80, 0
	s_and_saveexec_b64 s[10:11], vcc
	v_mov_b32_e32 v80, v149
	s_or_b64 exec, exec, s[10:11]

.LBB0_1776:
	s_cmp_lt_i32 s8, s6
	s_cselect_b64 s[0:1], -1, 0
	s_cmp_gt_i32 s8, s14
	s_cselect_b64 s[2:3], -1, 0
	s_or_b64 s[0:1], s[0:1], s[2:3]
	s_and_b64 vcc, exec, s[0:1]
	s_cbranch_vccnz .LBB0_1780
	ds_read_b128 v[96:99], v199
	ds_read_b128 v[224:227], v199 offset:32
	ds_read_b128 v[228:231], v199 offset:64
	ds_read_b128 v[248:251], v199 offset:96
	ds_read_b64_tr_b16 v[232:233], v200 offset:4608
	ds_read_b64_tr_b16 v[234:235], v200 offset:5120
	ds_read_b64_tr_b16 v[236:237], v200 offset:5632
	ds_read_b64_tr_b16 v[238:239], v200 offset:6144
	ds_read_b64_tr_b16 v[240:241], v200 offset:6656
	ds_read_b64_tr_b16 v[242:243], v200 offset:7168
	ds_read_b64_tr_b16 v[244:245], v200 offset:7680
	ds_read_b64_tr_b16 v[246:247], v200 offset:8192
	s_add_i32 s0, s7, 31
	s_cmp_gt_i32 s0, s15
	s_cselect_b64 s[0:1], -1, 0
	s_cmp_lt_i32 s7, s5
	s_cselect_b64 s[2:3], -1, 0
	s_or_b64 s[2:3], s[0:1], s[2:3]
	s_and_b64 vcc, exec, s[2:3]
	s_waitcnt lgkmcnt(11)
	v_mfma_f32_32x32x16_bf16 v[112:127], v[96:99], v[128:131], 0
	s_waitcnt lgkmcnt(10)
	v_mfma_f32_32x32x16_bf16 v[112:127], v[224:227], v[132:135], v[112:127]
	s_waitcnt lgkmcnt(9)
	v_mfma_f32_32x32x16_bf16 v[112:127], v[228:231], v[136:139], v[112:127]
	s_waitcnt lgkmcnt(8)
	v_mfma_f32_32x32x16_bf16 v[112:127], v[248:251], v[140:143], v[112:127]
	s_cbranch_vccnz .LBB0_1781
	s_mov_b32 s0, 0xff800000
	v_cmp_eq_f32_e32 vcc, s0, v202
	s_nop 1
	v_cndmask_b32_e64 v111, -v202, v192, vcc
	s_nop 5
	v_fmamk_f32 v96, v112, 0x3e38aa3b, v111
	v_exp_f32_e32 v96, v96
	v_fmamk_f32 v97, v113, 0x3e38aa3b, v111
	v_exp_f32_e32 v97, v97
	v_fmamk_f32 v98, v114, 0x3e38aa3b, v111
	v_exp_f32_e32 v98, v98
	v_fmamk_f32 v99, v115, 0x3e38aa3b, v111
	v_exp_f32_e32 v99, v99
	v_add_f32_e32 v100, 0, v96
	v_add_f32_e32 v100, v97, v100
	v_add_f32_e32 v100, v98, v100
	v_add_f32_e32 v104, v99, v100
	v_fmamk_f32 v100, v116, 0x3e38aa3b, v111
	v_exp_f32_e32 v100, v100
	v_fmamk_f32 v101, v117, 0x3e38aa3b, v111
	v_exp_f32_e32 v101, v101
	v_fmamk_f32 v102, v118, 0x3e38aa3b, v111
	v_exp_f32_e32 v102, v102
	v_fmamk_f32 v103, v119, 0x3e38aa3b, v111
	v_exp_f32_e32 v103, v103
	v_add_f32_e32 v104, v100, v104
	v_add_f32_e32 v104, v101, v104
	v_add_f32_e32 v104, v102, v104
	v_add_f32_e32 v108, v103, v104
	v_fmamk_f32 v104, v120, 0x3e38aa3b, v111
	v_exp_f32_e32 v104, v104
	v_fmamk_f32 v105, v121, 0x3e38aa3b, v111
	v_exp_f32_e32 v105, v105
	v_fmamk_f32 v106, v122, 0x3e38aa3b, v111
	v_exp_f32_e32 v106, v106
	v_fmamk_f32 v107, v123, 0x3e38aa3b, v111
	v_exp_f32_e32 v107, v107
	v_add_f32_e32 v108, v104, v108
	v_add_f32_e32 v108, v105, v108
	v_add_f32_e32 v108, v106, v108
	v_add_f32_e32 v203, v107, v108
	v_fmamk_f32 v108, v124, 0x3e38aa3b, v111
	v_exp_f32_e32 v108, v108
	v_fmamk_f32 v109, v125, 0x3e38aa3b, v111
	v_exp_f32_e32 v109, v109
	v_fmamk_f32 v110, v126, 0x3e38aa3b, v111
	v_exp_f32_e32 v110, v110
	v_fmac_f32_e32 v111, 0x3e38aa3b, v127
	v_exp_f32_e32 v111, v111
	v_add_f32_e32 v203, v108, v203
	v_add_f32_e32 v203, v109, v203
	v_add_f32_e32 v203, v110, v203
	v_add_f32_e32 v204, v111, v203
	v_cmp_nge_f32_e64 s[0:1], s26, v204
	s_or_b64 s[0:1], vcc, s[0:1]
	s_nop 0
	v_cndmask_b32_e64 v203, 0, 1, s[0:1]
	v_cmp_ne_u32_e32 vcc, 0, v203
	s_cmp_lg_u64 vcc, 0
	s_cselect_b64 s[0:1], -1, 0
	s_andn2_b64 vcc, exec, s[0:1]
	s_cbranch_vccz .LBB0_1782
	v_mov_b32_e32 v203, v202
	s_branch .LBB0_1791

.LBB0_1791:
	v_cvt_pk_bf16_f32 v96, v96, v97
	v_cvt_pk_bf16_f32 v97, v98, v99
	v_cvt_pk_bf16_f32 v98, v100, v101
	v_cvt_pk_bf16_f32 v100, v104, v105
	v_cvt_pk_bf16_f32 v101, v106, v107
	v_cvt_pk_bf16_f32 v99, v102, v103
	v_cvt_pk_bf16_f32 v102, v108, v109
	v_cvt_pk_bf16_f32 v103, v110, v111
	s_waitcnt lgkmcnt(6)
	v_mfma_f32_32x32x16_bf16 v[80:95], v[232:235], v[96:99], v[80:95]
	v_add_f32_e32 v195, v195, v204
	s_waitcnt lgkmcnt(4)
	v_mfma_f32_32x32x16_bf16 v[80:95], v[236:239], v[100:103], v[80:95]
	s_waitcnt lgkmcnt(2)
	v_mfma_f32_32x32x16_bf16 v[64:79], v[240:243], v[96:99], v[64:79]
	s_waitcnt lgkmcnt(0)
	v_mfma_f32_32x32x16_bf16 v[64:79], v[244:247], v[100:103], v[64:79]
.LBB0_1792:
	s_add_i32 s0, s4, 3
	s_min_i32 s0, s0, s16
	s_lshl_b32 s2, s0, 1
	s_waitcnt vmcnt(3)
	ds_write_b128 v197, v[144:147] offset:34816
	s_waitcnt vmcnt(2)
	ds_write_b128 v198, v[148:151] offset:39424
	s_waitcnt vmcnt(1)
	ds_write_b128 v197, v[152:155] offset:43520
	s_waitcnt vmcnt(0)
	ds_write_b128 v198, v[156:159] offset:48128
	v_mad_i64_i32 v[96:97], s[0:1], s2, v191, v[186:187]
	v_mad_i64_i32 v[98:99], s[0:1], s2, v191, v[188:189]
	s_or_b32 s2, s2, 1
	global_load_dwordx4 v[144:147], v[96:97], off
	global_load_dwordx4 v[148:151], v[98:99], off
	v_mad_i64_i32 v[96:97], s[0:1], s2, v191, v[186:187]
	v_mad_i64_i32 v[98:99], s[0:1], s2, v191, v[188:189]
	global_load_dwordx4 v[152:155], v[96:97], off
	global_load_dwordx4 v[156:159], v[98:99], off
	s_add_i32 s0, s8, 1
	s_cmp_lt_i32 s0, s6
	s_cselect_b64 s[0:1], -1, 0
	s_cmp_ge_i32 s8, s14
	s_cselect_b64 s[2:3], -1, 0
	s_or_b64 s[0:1], s[2:3], s[0:1]
	s_and_b64 vcc, exec, s[0:1]
	s_cbranch_vccnz .LBB0_1796
	ds_read_b128 v[96:99], v199 offset:8704
	ds_read_b128 v[100:103], v199 offset:8736
	ds_read_b128 v[224:227], v199 offset:8768
	ds_read_b128 v[228:231], v199 offset:8800
	ds_read_b64_tr_b16 v[232:233], v200 offset:13312
	ds_read_b64_tr_b16 v[234:235], v200 offset:13824
	ds_read_b64_tr_b16 v[236:237], v200 offset:14336
	ds_read_b64_tr_b16 v[238:239], v200 offset:14848
	ds_read_b64_tr_b16 v[240:241], v200 offset:15360
	ds_read_b64_tr_b16 v[242:243], v200 offset:15872
	ds_read_b64_tr_b16 v[244:245], v200 offset:16384
	ds_read_b64_tr_b16 v[246:247], v200 offset:16896
	s_add_i32 s2, s7, 32
	s_add_i32 s0, s7, 63
	s_cmp_gt_i32 s0, s15
	s_waitcnt lgkmcnt(11)
	v_mfma_f32_32x32x16_bf16 v[112:127], v[96:99], v[128:131], 0
	s_cselect_b64 s[0:1], -1, 0
	s_cmp_lt_i32 s2, s5
	s_cselect_b64 s[2:3], -1, 0
	s_or_b64 s[2:3], s[0:1], s[2:3]
	s_and_b64 vcc, exec, s[2:3]
	s_waitcnt lgkmcnt(10)
	v_mfma_f32_32x32x16_bf16 v[112:127], v[100:103], v[132:135], v[112:127]
	s_waitcnt lgkmcnt(9)
	v_mfma_f32_32x32x16_bf16 v[112:127], v[224:227], v[136:139], v[112:127]
	s_waitcnt lgkmcnt(8)
	v_mfma_f32_32x32x16_bf16 v[112:127], v[228:231], v[140:143], v[112:127]
	s_cbranch_vccnz .LBB0_1797
	s_mov_b32 s0, 0xff800000
	v_cmp_eq_f32_e32 vcc, s0, v203
	s_nop 1
	v_cndmask_b32_e64 v111, -v203, v192, vcc
	s_nop 5
	v_fmamk_f32 v96, v112, 0x3e38aa3b, v111
	v_exp_f32_e32 v96, v96
	v_fmamk_f32 v97, v113, 0x3e38aa3b, v111
	v_exp_f32_e32 v97, v97
	v_fmamk_f32 v98, v114, 0x3e38aa3b, v111
	v_exp_f32_e32 v98, v98
	v_fmamk_f32 v99, v115, 0x3e38aa3b, v111
	v_exp_f32_e32 v99, v99
	v_add_f32_e32 v100, 0, v96
	v_add_f32_e32 v100, v97, v100
	v_add_f32_e32 v100, v98, v100
	v_add_f32_e32 v104, v99, v100
	v_fmamk_f32 v100, v116, 0x3e38aa3b, v111
	v_exp_f32_e32 v100, v100
	v_fmamk_f32 v101, v117, 0x3e38aa3b, v111
	v_exp_f32_e32 v101, v101
	v_fmamk_f32 v102, v118, 0x3e38aa3b, v111
	v_exp_f32_e32 v102, v102
	v_fmamk_f32 v103, v119, 0x3e38aa3b, v111
	v_exp_f32_e32 v103, v103
	v_add_f32_e32 v104, v100, v104
	v_add_f32_e32 v104, v101, v104
	v_add_f32_e32 v104, v102, v104
	v_add_f32_e32 v108, v103, v104
	v_fmamk_f32 v104, v120, 0x3e38aa3b, v111
	v_exp_f32_e32 v104, v104
	v_fmamk_f32 v105, v121, 0x3e38aa3b, v111
	v_exp_f32_e32 v105, v105
	v_fmamk_f32 v106, v122, 0x3e38aa3b, v111
	v_exp_f32_e32 v106, v106
	v_fmamk_f32 v107, v123, 0x3e38aa3b, v111
	v_exp_f32_e32 v107, v107
	v_add_f32_e32 v108, v104, v108
	v_add_f32_e32 v108, v105, v108
	v_add_f32_e32 v108, v106, v108
	v_add_f32_e32 v202, v107, v108
	v_fmamk_f32 v108, v124, 0x3e38aa3b, v111
	v_exp_f32_e32 v108, v108
	v_fmamk_f32 v109, v125, 0x3e38aa3b, v111
	v_exp_f32_e32 v109, v109
	v_fmamk_f32 v110, v126, 0x3e38aa3b, v111
	v_exp_f32_e32 v110, v110
	v_fmac_f32_e32 v111, 0x3e38aa3b, v127
	v_exp_f32_e32 v111, v111
	v_add_f32_e32 v202, v108, v202
	v_add_f32_e32 v202, v109, v202
	v_add_f32_e32 v202, v110, v202
	v_add_f32_e32 v204, v111, v202
	v_cmp_nge_f32_e64 s[0:1], s26, v204
	s_or_b64 s[0:1], vcc, s[0:1]
	s_nop 0
	v_cndmask_b32_e64 v202, 0, 1, s[0:1]
	v_cmp_ne_u32_e32 vcc, 0, v202
	s_cmp_lg_u64 vcc, 0
	s_cselect_b64 s[0:1], -1, 0
	s_andn2_b64 vcc, exec, s[0:1]
	s_cbranch_vccz .LBB0_1798
	v_mov_b32_e32 v202, v203
	s_branch .LBB0_1807

.LBB0_1808:
	s_cmp_ge_i32 s4, s16
	s_waitcnt lgkmcnt(0)
	s_barrier
	s_cbranch_scc1 .LBB0_1775
	s_add_i32 s9, s8, 2
	s_cmp_lt_i32 s9, s6
	s_cselect_b64 s[0:1], -1, 0
	s_cmp_gt_i32 s9, s14
	s_cselect_b64 s[2:3], -1, 0
	s_or_b64 s[0:1], s[0:1], s[2:3]
	s_and_b64 vcc, exec, s[0:1]
	s_cbranch_vccnz .LBB0_1813
	ds_read_b128 v[96:99], v199 offset:34816
	ds_read_b128 v[100:103], v199 offset:34848
	ds_read_b128 v[224:227], v199 offset:34880
	ds_read_b128 v[228:231], v199 offset:34912
	ds_read_b64_tr_b16 v[232:233], v200 offset:39424
	ds_read_b64_tr_b16 v[234:235], v200 offset:39936
	ds_read_b64_tr_b16 v[236:237], v200 offset:40448
	ds_read_b64_tr_b16 v[238:239], v200 offset:40960
	ds_read_b64_tr_b16 v[240:241], v200 offset:41472
	ds_read_b64_tr_b16 v[242:243], v200 offset:41984
	ds_read_b64_tr_b16 v[244:245], v200 offset:42496
	ds_read_b64_tr_b16 v[246:247], v200 offset:43008
	s_add_i32 s2, s7, 64
	s_add_i32 s0, s7, 0x5f
	s_cmp_gt_i32 s0, s15
	s_waitcnt lgkmcnt(11)
	v_mfma_f32_32x32x16_bf16 v[112:127], v[96:99], v[128:131], 0
	s_cselect_b64 s[0:1], -1, 0
	s_cmp_lt_i32 s2, s5
	s_cselect_b64 s[2:3], -1, 0
	s_or_b64 s[2:3], s[0:1], s[2:3]
	s_and_b64 vcc, exec, s[2:3]
	s_waitcnt lgkmcnt(10)
	v_mfma_f32_32x32x16_bf16 v[112:127], v[100:103], v[132:135], v[112:127]
	s_waitcnt lgkmcnt(9)
	v_mfma_f32_32x32x16_bf16 v[112:127], v[224:227], v[136:139], v[112:127]
	s_waitcnt lgkmcnt(8)
	v_mfma_f32_32x32x16_bf16 v[112:127], v[228:231], v[140:143], v[112:127]
	s_cbranch_vccnz .LBB0_1818
	s_mov_b32 s0, 0xff800000
	v_cmp_eq_f32_e32 vcc, s0, v202
	s_nop 1
	v_cndmask_b32_e64 v111, -v202, v192, vcc
	s_nop 5
	v_fmamk_f32 v96, v112, 0x3e38aa3b, v111
	v_exp_f32_e32 v96, v96
	v_fmamk_f32 v97, v113, 0x3e38aa3b, v111
	v_exp_f32_e32 v97, v97
	v_fmamk_f32 v98, v114, 0x3e38aa3b, v111
	v_exp_f32_e32 v98, v98
	v_fmamk_f32 v99, v115, 0x3e38aa3b, v111
	v_exp_f32_e32 v99, v99
	v_add_f32_e32 v100, 0, v96
	v_add_f32_e32 v100, v97, v100
	v_add_f32_e32 v100, v98, v100
	v_add_f32_e32 v104, v99, v100
	v_fmamk_f32 v100, v116, 0x3e38aa3b, v111
	v_exp_f32_e32 v100, v100
	v_fmamk_f32 v101, v117, 0x3e38aa3b, v111
	v_exp_f32_e32 v101, v101
	v_fmamk_f32 v102, v118, 0x3e38aa3b, v111
	v_exp_f32_e32 v102, v102
	v_fmamk_f32 v103, v119, 0x3e38aa3b, v111
	v_exp_f32_e32 v103, v103
	v_add_f32_e32 v104, v100, v104
	v_add_f32_e32 v104, v101, v104
	v_add_f32_e32 v104, v102, v104
	v_add_f32_e32 v108, v103, v104
	v_fmamk_f32 v104, v120, 0x3e38aa3b, v111
	v_exp_f32_e32 v104, v104
	v_fmamk_f32 v105, v121, 0x3e38aa3b, v111
	v_exp_f32_e32 v105, v105
	v_fmamk_f32 v106, v122, 0x3e38aa3b, v111
	v_exp_f32_e32 v106, v106
	v_fmamk_f32 v107, v123, 0x3e38aa3b, v111
	v_exp_f32_e32 v107, v107
	v_add_f32_e32 v108, v104, v108
	v_add_f32_e32 v108, v105, v108
	v_add_f32_e32 v108, v106, v108
	v_add_f32_e32 v203, v107, v108
	v_fmamk_f32 v108, v124, 0x3e38aa3b, v111
	v_exp_f32_e32 v108, v108
	v_fmamk_f32 v109, v125, 0x3e38aa3b, v111
	v_exp_f32_e32 v109, v109
	v_fmamk_f32 v110, v126, 0x3e38aa3b, v111
	v_exp_f32_e32 v110, v110
	v_fmac_f32_e32 v111, 0x3e38aa3b, v127
	v_exp_f32_e32 v111, v111
	v_add_f32_e32 v203, v108, v203
	v_add_f32_e32 v203, v109, v203
	v_add_f32_e32 v203, v110, v203
	v_add_f32_e32 v204, v111, v203
	v_cmp_nge_f32_e64 s[0:1], s26, v204
	s_or_b64 s[0:1], vcc, s[0:1]
	s_nop 0
	v_cndmask_b32_e64 v203, 0, 1, s[0:1]
	v_cmp_ne_u32_e32 vcc, 0, v203
	s_cmp_lg_u64 vcc, 0
	s_cselect_b64 s[0:1], -1, 0
	s_andn2_b64 vcc, exec, s[0:1]
	s_cbranch_vccz .LBB0_1819
	v_mov_b32_e32 v203, v202
	s_branch .LBB0_1828

.LBB0_1829:
	s_add_i32 s0, s4, 4
	s_min_i32 s0, s0, s16
	s_lshl_b32 s2, s0, 1
	s_waitcnt vmcnt(7)
	ds_write_b128 v197, v[160:163]
	s_waitcnt vmcnt(6)
	ds_write_b128 v198, v[164:167] offset:4608
	s_waitcnt vmcnt(5)
	ds_write_b128 v197, v[168:171] offset:8704
	s_waitcnt vmcnt(4)
	ds_write_b128 v198, v[172:175] offset:13312
	v_mad_i64_i32 v[96:97], s[0:1], s2, v191, v[186:187]
	v_mad_i64_i32 v[98:99], s[0:1], s2, v191, v[188:189]
	s_or_b32 s2, s2, 1
	global_load_dwordx4 v[160:163], v[96:97], off
	global_load_dwordx4 v[164:167], v[98:99], off
	v_mad_i64_i32 v[96:97], s[0:1], s2, v191, v[186:187]
	v_mad_i64_i32 v[98:99], s[0:1], s2, v191, v[188:189]
	global_load_dwordx4 v[168:171], v[96:97], off
	global_load_dwordx4 v[172:175], v[98:99], off
	s_add_i32 s0, s8, 3
	s_cmp_lt_i32 s0, s6
	s_cselect_b64 s[0:1], -1, 0
	s_cmp_ge_i32 s9, s14
	s_cselect_b64 s[2:3], -1, 0
	s_or_b64 s[0:1], s[2:3], s[0:1]
	s_and_b64 vcc, exec, s[0:1]
	s_cbranch_vccnz .LBB0_1833
	ds_read_b128 v[96:99], v199 offset:43520
	ds_read_b128 v[100:103], v199 offset:43552
	ds_read_b128 v[224:227], v199 offset:43584
	ds_read_b128 v[228:231], v199 offset:43616
	ds_read_b64_tr_b16 v[232:233], v200 offset:48128
	ds_read_b64_tr_b16 v[234:235], v200 offset:48640
	ds_read_b64_tr_b16 v[236:237], v200 offset:49152
	ds_read_b64_tr_b16 v[238:239], v200 offset:49664
	ds_read_b64_tr_b16 v[240:241], v200 offset:50176
	ds_read_b64_tr_b16 v[242:243], v200 offset:50688
	ds_read_b64_tr_b16 v[244:245], v200 offset:51200
	ds_read_b64_tr_b16 v[246:247], v200 offset:51712
	s_add_i32 s2, s7, 0x60
	s_add_i32 s0, s7, 0x7f
	s_cmp_gt_i32 s0, s15
	s_waitcnt lgkmcnt(11)
	v_mfma_f32_32x32x16_bf16 v[112:127], v[96:99], v[128:131], 0
	s_cselect_b64 s[0:1], -1, 0
	s_cmp_lt_i32 s2, s5
	s_cselect_b64 s[2:3], -1, 0
	s_or_b64 s[2:3], s[0:1], s[2:3]
	s_and_b64 vcc, exec, s[2:3]
	s_waitcnt lgkmcnt(10)
	v_mfma_f32_32x32x16_bf16 v[112:127], v[100:103], v[132:135], v[112:127]
	s_waitcnt lgkmcnt(9)
	v_mfma_f32_32x32x16_bf16 v[112:127], v[224:227], v[136:139], v[112:127]
	s_waitcnt lgkmcnt(8)
	v_mfma_f32_32x32x16_bf16 v[112:127], v[228:231], v[140:143], v[112:127]
	s_cbranch_vccnz .LBB0_1834
	s_mov_b32 s0, 0xff800000
	v_cmp_eq_f32_e32 vcc, s0, v203
	s_nop 1
	v_cndmask_b32_e64 v111, -v203, v192, vcc
	s_nop 5
	v_fmamk_f32 v96, v112, 0x3e38aa3b, v111
	v_exp_f32_e32 v96, v96
	v_fmamk_f32 v97, v113, 0x3e38aa3b, v111
	v_exp_f32_e32 v97, v97
	v_fmamk_f32 v98, v114, 0x3e38aa3b, v111
	v_exp_f32_e32 v98, v98
	v_fmamk_f32 v99, v115, 0x3e38aa3b, v111
	v_exp_f32_e32 v99, v99
	v_add_f32_e32 v100, 0, v96
	v_add_f32_e32 v100, v97, v100
	v_add_f32_e32 v100, v98, v100
	v_add_f32_e32 v104, v99, v100
	v_fmamk_f32 v100, v116, 0x3e38aa3b, v111
	v_exp_f32_e32 v100, v100
	v_fmamk_f32 v101, v117, 0x3e38aa3b, v111
	v_exp_f32_e32 v101, v101
	v_fmamk_f32 v102, v118, 0x3e38aa3b, v111
	v_exp_f32_e32 v102, v102
	v_fmamk_f32 v103, v119, 0x3e38aa3b, v111
	v_exp_f32_e32 v103, v103
	v_add_f32_e32 v104, v100, v104
	v_add_f32_e32 v104, v101, v104
	v_add_f32_e32 v104, v102, v104
	v_add_f32_e32 v108, v103, v104
	v_fmamk_f32 v104, v120, 0x3e38aa3b, v111
	v_exp_f32_e32 v104, v104
	v_fmamk_f32 v105, v121, 0x3e38aa3b, v111
	v_exp_f32_e32 v105, v105
	v_fmamk_f32 v106, v122, 0x3e38aa3b, v111
	v_exp_f32_e32 v106, v106
	v_fmamk_f32 v107, v123, 0x3e38aa3b, v111
	v_exp_f32_e32 v107, v107
	v_add_f32_e32 v108, v104, v108
	v_add_f32_e32 v108, v105, v108
	v_add_f32_e32 v108, v106, v108
	v_add_f32_e32 v202, v107, v108
	v_fmamk_f32 v108, v124, 0x3e38aa3b, v111
	v_exp_f32_e32 v108, v108
	v_fmamk_f32 v109, v125, 0x3e38aa3b, v111
	v_exp_f32_e32 v109, v109
	v_fmamk_f32 v110, v126, 0x3e38aa3b, v111
	v_exp_f32_e32 v110, v110
	v_fmac_f32_e32 v111, 0x3e38aa3b, v127
	v_exp_f32_e32 v111, v111
	v_add_f32_e32 v202, v108, v202
	v_add_f32_e32 v202, v109, v202
	v_add_f32_e32 v202, v110, v202
	v_add_f32_e32 v204, v111, v202
	v_cmp_nge_f32_e64 s[0:1], s26, v204
	s_or_b64 s[0:1], vcc, s[0:1]
	s_nop 0
	v_cndmask_b32_e64 v202, 0, 1, s[0:1]
	v_cmp_ne_u32_e32 vcc, 0, v202
	s_cmp_lg_u64 vcc, 0
	s_cselect_b64 s[0:1], -1, 0
	s_andn2_b64 vcc, exec, s[0:1]
	s_cbranch_vccz .LBB0_1835
	v_mov_b32_e32 v202, v203
	s_branch .LBB0_1844
